# stream: enc loads with sc0 sc1 nt (system-scope non-temporal) instead of nt; early barrier + rotated wave-row kept
# baseline (speedup 1.0000x reference)
.LBB1_2:
	s_or_b64 exec, exec, s[0:1]
	s_lshr_b32 s8, s3, 6
	s_add_i32 s8, s8, s2
	s_and_b32 s8, s8, 15
	s_lshl_b32 s0, s2, 7
	v_and_b32_e32 v24, 63, v0
	s_add_i32 s9, s8, s0
	s_waitcnt lgkmcnt(0)
	s_and_b32 s1, s5, 0xffff
	s_mov_b32 s3, 0x20000
	s_brev_b32 s2, 16
	s_mov_b32 s0, s4
	v_lshlrev_b32_e32 v25, 4, v24
	s_lshl_b32 s4, s9, 12
	buffer_load_dwordx4 v[26:29], v25, s[0:3], s4 offen offset:1024 sc0 sc1 nt
	buffer_load_dwordx4 v[30:33], v25, s[0:3], s4 offen sc0 sc1 nt
	buffer_load_dwordx4 v[34:37], v25, s[0:3], s4 offen offset:2048 sc0 sc1 nt
	s_barrier
	s_add_i32 s5, s4, 0x10000
	buffer_load_dwordx4 v[38:41], v25, s[0:3], s5 offen offset:1024 sc0 sc1 nt
	buffer_load_dwordx4 v[42:45], v25, s[0:3], s5 offen sc0 sc1 nt
	buffer_load_dwordx4 v[16:19], v25, s[0:3], s4 offen offset:3072 sc0 sc1 nt
	s_add_i32 s10, s4, 0x20000
	buffer_load_dwordx4 v[46:49], v25, s[0:3], s5 offen offset:2048 sc0 sc1 nt
	buffer_load_dwordx4 v[20:23], v25, s[0:3], s5 offen offset:3072 sc0 sc1 nt
	buffer_load_dwordx4 v[50:53], v25, s[0:3], s10 offen offset:1024 sc0 sc1 nt
	buffer_load_dwordx4 v[54:57], v25, s[0:3], s10 offen sc0 sc1 nt
	ds_read_b128 v[4:7], v25 offset:1024
	ds_read_b128 v[0:3], v25
	ds_read_b128 v[12:15], v25 offset:2048
	ds_read_b128 v[8:11], v25 offset:3072
	s_add_i32 s5, s4, 0x30000
	v_cmp_gt_u32_e32 vcc, 8, v24
	s_waitcnt vmcnt(9) lgkmcnt(3)
	v_pk_mul_f32 v[28:29], v[6:7], v[28:29]
	v_pk_mul_f32 v[26:27], v[4:5], v[26:27]
	s_waitcnt vmcnt(8) lgkmcnt(2)
	v_pk_fma_f32 v[32:33], v[2:3], v[32:33], v[28:29]
	v_pk_fma_f32 v[30:31], v[0:1], v[30:31], v[26:27]
	buffer_load_dwordx4 v[26:29], v25, s[0:3], s5 offen offset:1024 sc0 sc1 nt
	s_waitcnt vmcnt(8) lgkmcnt(1)
	v_pk_fma_f32 v[58:59], v[14:15], v[36:37], v[32:33]
	v_pk_fma_f32 v[60:61], v[12:13], v[34:35], v[30:31]
	buffer_load_dwordx4 v[30:33], v25, s[0:3], s5 offen sc0 sc1 nt
	s_waitcnt vmcnt(8)
	v_pk_mul_f32 v[34:35], v[6:7], v[40:41]
	v_pk_mul_f32 v[36:37], v[4:5], v[38:39]
	s_waitcnt vmcnt(7)
	v_pk_fma_f32 v[44:45], v[2:3], v[44:45], v[34:35]
	v_pk_fma_f32 v[42:43], v[0:1], v[42:43], v[36:37]
	buffer_load_dwordx4 v[34:37], v25, s[0:3], s10 offen offset:2048 sc0 sc1 nt
	s_waitcnt vmcnt(4)
	v_pk_mul_f32 v[38:39], v[6:7], v[52:53]
	v_pk_mul_f32 v[40:41], v[4:5], v[50:51]
	s_waitcnt vmcnt(3)
	v_pk_fma_f32 v[50:51], v[2:3], v[56:57], v[38:39]
	v_pk_fma_f32 v[52:53], v[0:1], v[54:55], v[40:41]
	buffer_load_dwordx4 v[38:41], v25, s[0:3], s10 offen offset:3072 sc0 sc1 nt
	v_pk_fma_f32 v[48:49], v[14:15], v[48:49], v[44:45]
	v_pk_fma_f32 v[46:47], v[12:13], v[46:47], v[42:43]
	s_waitcnt lgkmcnt(0)
	v_pk_fma_f32 v[18:19], v[10:11], v[18:19], v[58:59]
	v_pk_fma_f32 v[16:17], v[8:9], v[16:17], v[60:61]
	v_add_f32_e32 v61, v18, v19
	v_add_f32_e32 v60, v16, v17
	v_pk_fma_f32 v[16:17], v[10:11], v[22:23], v[48:49]
	v_pk_fma_f32 v[18:19], v[8:9], v[20:21], v[46:47]
	v_add_f32_e32 v16, v16, v17
	v_add_f32_e32 v18, v18, v19
	v_add_f32_e32 v60, v60, v61
	v_add_f32_e32 v16, v18, v16
	s_add_i32 s10, s4, 0x50000
	s_waitcnt vmcnt(3)
	v_pk_mul_f32 v[28:29], v[6:7], v[28:29]
	v_pk_mul_f32 v[26:27], v[4:5], v[26:27]
	v_add_f32_dpp v16, v16, v16 quad_perm:[1,0,3,2] row_mask:0xf bank_mask:0xf bound_ctrl:1
	s_waitcnt vmcnt(2)
	v_pk_fma_f32 v[54:55], v[2:3], v[32:33], v[28:29]
	v_pk_fma_f32 v[56:57], v[0:1], v[30:31], v[26:27]
	buffer_load_dwordx4 v[26:29], v25, s[0:3], s5 offen offset:2048 sc0 sc1 nt
	buffer_load_dwordx4 v[30:33], v25, s[0:3], s5 offen offset:3072 sc0 sc1 nt
	s_add_i32 s5, s4, 0x40000
	buffer_load_dwordx4 v[42:45], v25, s[0:3], s5 offen offset:1024 sc0 sc1 nt
	s_waitcnt vmcnt(4)
	v_pk_fma_f32 v[50:51], v[14:15], v[36:37], v[50:51]
	v_pk_fma_f32 v[52:53], v[12:13], v[34:35], v[52:53]
	buffer_load_dwordx4 v[34:37], v25, s[0:3], s5 offen sc0 sc1 nt
	v_add_f32_dpp v16, v16, v16 quad_perm:[2,3,0,1] row_mask:0xf bank_mask:0xf bound_ctrl:1
	s_waitcnt vmcnt(4)
	v_pk_fma_f32 v[58:59], v[10:11], v[40:41], v[50:51]
	v_pk_fma_f32 v[38:39], v[8:9], v[38:39], v[52:53]
	v_add_f32_e32 v19, v58, v59
	v_add_f32_e32 v17, v38, v39
	v_add_f32_dpp v58, v60, v60 quad_perm:[1,0,3,2] row_mask:0xf bank_mask:0xf bound_ctrl:1
	v_add_f32_e32 v18, v17, v19
	v_add_f32_dpp v16, v16, v16 row_ror:4 row_mask:0xf bank_mask:0xf bound_ctrl:1
	v_add_f32_dpp v17, v58, v58 quad_perm:[2,3,0,1] row_mask:0xf bank_mask:0xf bound_ctrl:1
	buffer_load_dwordx4 v[20:23], v25, s[0:3], s5 offen offset:2048 sc0 sc1 nt
	buffer_load_dwordx4 v[46:49], v25, s[0:3], s5 offen offset:3072 sc0 sc1 nt
	v_add_f32_dpp v17, v17, v17 row_ror:4 row_mask:0xf bank_mask:0xf bound_ctrl:1
	v_add_f32_dpp v58, v16, v16 row_ror:8 row_mask:0xf bank_mask:0xf bound_ctrl:1
	buffer_load_dwordx4 v[38:41], v25, s[0:3], s10 offen sc0 sc1 nt
	buffer_load_dwordx4 v[50:53], v25, s[0:3], s10 offen offset:1024 sc0 sc1 nt
	v_add_f32_dpp v17, v17, v17 row_ror:8 row_mask:0xf bank_mask:0xf bound_ctrl:1
	v_mov_b32_e32 v19, v17
	v_mov_b32_e32 v59, v58
	s_nop 0
	v_permlane16_swap_b32_e32 v17, v19
	v_permlane16_swap_b32_e32 v58, v59
	v_add_f32_e32 v16, v17, v19
	v_add_f32_e32 v17, v58, v59
	s_add_i32 s5, s4, 0x60000
	s_add_i32 s4, s4, 0x70000
	v_add_f32_dpp v18, v18, v18 quad_perm:[1,0,3,2] row_mask:0xf bank_mask:0xf bound_ctrl:1
	s_waitcnt vmcnt(7)
	v_pk_fma_f32 v[28:29], v[14:15], v[28:29], v[54:55]
	v_pk_fma_f32 v[54:55], v[12:13], v[26:27], v[56:57]
	s_waitcnt vmcnt(6)
	v_pk_fma_f32 v[58:59], v[10:11], v[32:33], v[28:29]
	buffer_load_dwordx4 v[26:29], v25, s[0:3], s10 offen offset:2048 sc0 sc1 nt
	v_pk_fma_f32 v[54:55], v[8:9], v[30:31], v[54:55]
	buffer_load_dwordx4 v[30:33], v25, s[0:3], s10 offen offset:3072 sc0 sc1 nt
	v_add_f32_e32 v66, v54, v55
	s_waitcnt vmcnt(7)
	v_pk_mul_f32 v[54:55], v[6:7], v[44:45]
	v_pk_mul_f32 v[56:57], v[4:5], v[42:43]
	buffer_load_dwordx4 v[42:45], v25, s[0:3], s5 offen offset:1024 sc0 sc1 nt
	s_waitcnt vmcnt(7)
	v_pk_fma_f32 v[54:55], v[2:3], v[36:37], v[54:55]
	v_pk_fma_f32 v[56:57], v[0:1], v[34:35], v[56:57]
	buffer_load_dwordx4 v[34:37], v25, s[0:3], s5 offen sc0 sc1 nt
	v_add_f32_dpp v18, v18, v18 quad_perm:[2,3,0,1] row_mask:0xf bank_mask:0xf bound_ctrl:1
	s_waitcnt vmcnt(7)
	v_pk_fma_f32 v[22:23], v[14:15], v[22:23], v[54:55]
	v_pk_fma_f32 v[20:21], v[12:13], v[20:21], v[56:57]
	s_waitcnt vmcnt(6)
	v_pk_fma_f32 v[60:61], v[10:11], v[48:49], v[22:23]
	v_pk_fma_f32 v[22:23], v[8:9], v[46:47], v[20:21]
	s_waitcnt vmcnt(4)
	v_pk_mul_f32 v[54:55], v[4:5], v[50:51]
	v_pk_mul_f32 v[20:21], v[6:7], v[52:53]
	v_pk_fma_f32 v[38:39], v[0:1], v[38:39], v[54:55]
	buffer_load_dwordx4 v[46:49], v25, s[0:3], s5 offen offset:2048 sc0 sc1 nt
	buffer_load_dwordx4 v[50:53], v25, s[0:3], s5 offen offset:3072 sc0 sc1 nt
	v_pk_fma_f32 v[20:21], v[2:3], v[40:41], v[20:21]
	v_add_f32_e32 v23, v22, v23
	v_add_f32_dpp v18, v18, v18 row_ror:4 row_mask:0xf bank_mask:0xf bound_ctrl:1
	s_waitcnt vmcnt(5)
	v_pk_fma_f32 v[26:27], v[12:13], v[26:27], v[38:39]
	buffer_load_dwordx4 v[38:41], v25, s[0:3], s4 offen sc0 sc1 nt
	buffer_load_dwordx4 v[54:57], v25, s[0:3], s4 offen offset:1024 sc0 sc1 nt
	v_pk_fma_f32 v[20:21], v[14:15], v[28:29], v[20:21]
	s_waitcnt vmcnt(6)
	v_pk_fma_f32 v[30:31], v[8:9], v[30:31], v[26:27]
	v_pk_fma_f32 v[62:63], v[10:11], v[32:33], v[20:21]
	v_add_f32_dpp v18, v18, v18 row_ror:8 row_mask:0xf bank_mask:0xf bound_ctrl:1
	s_waitcnt vmcnt(5)
	v_pk_mul_f32 v[20:21], v[6:7], v[44:45]
	v_pk_mul_f32 v[26:27], v[4:5], v[42:43]
	buffer_load_dwordx4 v[42:45], v25, s[0:3], s4 offen offset:2048 sc0 sc1 nt
	s_waitcnt vmcnt(5)
	v_pk_fma_f32 v[64:65], v[0:1], v[34:35], v[26:27]
	buffer_load_dwordx4 v[32:35], v25, s[0:3], s4 offen offset:3072 sc0 sc1 nt
	v_add_f32_e32 v27, v60, v61
	v_add_f32_e32 v23, v23, v27
	v_pk_fma_f32 v[36:37], v[2:3], v[36:37], v[20:21]
	v_add_f32_e32 v20, v58, v59
	v_add_f32_dpp v23, v23, v23 quad_perm:[1,0,3,2] row_mask:0xf bank_mask:0xf bound_ctrl:1
	v_add_f32_e32 v20, v66, v20
	v_mov_b32_e32 v19, v18
	v_add_f32_dpp v23, v23, v23 quad_perm:[2,3,0,1] row_mask:0xf bank_mask:0xf bound_ctrl:1
	v_add_f32_dpp v20, v20, v20 quad_perm:[1,0,3,2] row_mask:0xf bank_mask:0xf bound_ctrl:1
	v_permlane16_swap_b32_e32 v18, v19
	v_add_f32_dpp v23, v23, v23 row_ror:4 row_mask:0xf bank_mask:0xf bound_ctrl:1
	v_add_f32_dpp v20, v20, v20 quad_perm:[2,3,0,1] row_mask:0xf bank_mask:0xf bound_ctrl:1
	v_add_f32_e32 v18, v18, v19
	v_add_f32_dpp v23, v23, v23 row_ror:8 row_mask:0xf bank_mask:0xf bound_ctrl:1
	v_mov_b32_e32 v27, v23
	s_nop 1
	v_permlane16_swap_b32_e32 v23, v27
	v_add_f32_e32 v28, v23, v27
	v_add_f32_e32 v23, v30, v31
	s_waitcnt vmcnt(5)
	v_pk_fma_f32 v[30:31], v[14:15], v[48:49], v[36:37]
	v_pk_fma_f32 v[36:37], v[12:13], v[46:47], v[64:65]
	s_waitcnt vmcnt(4)
	v_pk_fma_f32 v[30:31], v[10:11], v[52:53], v[30:31]
	v_pk_fma_f32 v[36:37], v[8:9], v[50:51], v[36:37]
	v_add_f32_e32 v27, v62, v63
	v_add_f32_e32 v36, v36, v37
	v_add_f32_e32 v30, v30, v31
	v_add_f32_e32 v23, v23, v27
	v_add_f32_e32 v30, v36, v30
	v_add_f32_dpp v20, v20, v20 row_ror:4 row_mask:0xf bank_mask:0xf bound_ctrl:1
	v_add_f32_dpp v23, v23, v23 quad_perm:[1,0,3,2] row_mask:0xf bank_mask:0xf bound_ctrl:1
	v_add_f32_dpp v30, v30, v30 quad_perm:[1,0,3,2] row_mask:0xf bank_mask:0xf bound_ctrl:1
	v_add_f32_dpp v20, v20, v20 row_ror:8 row_mask:0xf bank_mask:0xf bound_ctrl:1
	v_add_f32_dpp v23, v23, v23 quad_perm:[2,3,0,1] row_mask:0xf bank_mask:0xf bound_ctrl:1
	v_add_f32_dpp v30, v30, v30 quad_perm:[2,3,0,1] row_mask:0xf bank_mask:0xf bound_ctrl:1
	v_mov_b32_e32 v21, v20
	v_add_f32_dpp v23, v23, v23 row_ror:4 row_mask:0xf bank_mask:0xf bound_ctrl:1
	v_add_f32_dpp v30, v30, v30 row_ror:4 row_mask:0xf bank_mask:0xf bound_ctrl:1
	v_permlane16_swap_b32_e32 v20, v21
	v_add_f32_dpp v23, v23, v23 row_ror:8 row_mask:0xf bank_mask:0xf bound_ctrl:1
	v_add_f32_dpp v30, v30, v30 row_ror:8 row_mask:0xf bank_mask:0xf bound_ctrl:1
	v_mov_b32_e32 v27, v23
	v_mov_b32_e32 v31, v30
	s_nop 0
	v_permlane16_swap_b32_e32 v23, v27
	v_permlane16_swap_b32_e32 v30, v31
	v_add_f32_e32 v21, v20, v21
	v_add_f32_e32 v23, v23, v27
	v_add_f32_e32 v30, v30, v31
	v_mov_b32_e32 v19, v16
	v_mov_b32_e32 v20, v17
	v_mov_b32_e32 v22, v18
	v_mov_b32_e32 v26, v21
	v_mov_b32_e32 v29, v28
	v_mov_b32_e32 v27, v23
	v_mov_b32_e32 v31, v30
	v_permlane32_swap_b32_e32 v16, v19
	v_permlane32_swap_b32_e32 v17, v20
	v_permlane32_swap_b32_e32 v18, v22
	v_permlane32_swap_b32_e32 v21, v26
	v_permlane32_swap_b32_e32 v28, v29
	v_permlane32_swap_b32_e32 v23, v27
	s_waitcnt vmcnt(2)
	v_pk_mul_f32 v[6:7], v[6:7], v[56:57]
	v_pk_mul_f32 v[4:5], v[4:5], v[54:55]
	v_pk_fma_f32 v[2:3], v[2:3], v[40:41], v[6:7]
	v_pk_fma_f32 v[0:1], v[0:1], v[38:39], v[4:5]
	v_permlane32_swap_b32_e32 v30, v31
	s_waitcnt vmcnt(1)
	v_pk_fma_f32 v[2:3], v[14:15], v[44:45], v[2:3]
	v_pk_fma_f32 v[0:1], v[12:13], v[42:43], v[0:1]
	s_waitcnt vmcnt(0)
	v_pk_fma_f32 v[2:3], v[10:11], v[34:35], v[2:3]
	v_pk_fma_f32 v[0:1], v[8:9], v[32:33], v[0:1]
	s_nop 0
	v_add_f32_e32 v0, v0, v1
	v_add_f32_e32 v1, v2, v3
	v_add_f32_e32 v0, v0, v1
	s_nop 1
	v_add_f32_dpp v0, v0, v0 quad_perm:[1,0,3,2] row_mask:0xf bank_mask:0xf bound_ctrl:1
	s_nop 1
	v_add_f32_dpp v0, v0, v0 quad_perm:[2,3,0,1] row_mask:0xf bank_mask:0xf bound_ctrl:1
	s_nop 1
	v_add_f32_dpp v0, v0, v0 row_ror:4 row_mask:0xf bank_mask:0xf bound_ctrl:1
	s_nop 1
	v_add_f32_dpp v0, v0, v0 row_ror:8 row_mask:0xf bank_mask:0xf bound_ctrl:1
	v_mov_b32_e32 v1, v0
	s_nop 1
	v_permlane16_swap_b32_e32 v0, v1
	v_add_f32_e32 v0, v0, v1
	v_mov_b32_e32 v1, v0
	s_nop 1
	v_permlane32_swap_b32_e32 v0, v1
	s_and_saveexec_b64 s[0:1], vcc
	s_cbranch_execz .LBB1_4
	v_add_f32_e32 v6, v16, v19
	v_cmp_eq_u32_e32 vcc, 0, v24
	v_add_f32_e32 v5, v17, v20
	v_add_f32_e32 v4, v18, v22
	v_cndmask_b32_e32 v6, 0, v6, vcc
	v_cmp_eq_u32_e32 vcc, 1, v24
	v_add_f32_e32 v3, v21, v26
	v_add_f32_e32 v2, v28, v29
	v_cndmask_b32_e32 v5, v6, v5, vcc
	v_cmp_eq_u32_e32 vcc, 2, v24
	v_add_f32_e32 v0, v0, v1
	v_add_f32_e32 v1, v30, v31
	v_cndmask_b32_e32 v4, v5, v4, vcc
	v_cmp_eq_u32_e32 vcc, 3, v24
	s_lshl_b32 s0, s8, 13
	s_and_b32 s0, s0, 0x1e000
	v_cndmask_b32_e32 v3, v4, v3, vcc
	v_cmp_eq_u32_e32 vcc, 4, v24
	s_add_u32 s0, s6, s0
	s_addc_u32 s1, s7, 0
	v_cndmask_b32_e32 v2, v3, v2, vcc
	v_add_f32_e32 v3, v23, v27
	v_cmp_eq_u32_e32 vcc, 5, v24
	s_nop 1
	v_cndmask_b32_e32 v2, v2, v3, vcc
	v_cmp_eq_u32_e32 vcc, 6, v24
	s_nop 1
	v_cndmask_b32_e32 v1, v2, v1, vcc
	v_cmp_eq_u32_e32 vcc, 7, v24
	s_nop 1
	v_cndmask_b32_e32 v2, v1, v0, vcc
	v_add_u32_e32 v0, s9, v25
	v_ashrrev_i32_e32 v0, 4, v0
	v_ashrrev_i32_e32 v1, 31, v0
	v_lshl_add_u64 v[0:1], v[0:1], 2, s[0:1]
	v_add_co_u32_e32 v0, vcc, 0x6000, v0
	s_nop 1
	v_addc_co_u32_e32 v1, vcc, 0, v1, vcc
	global_store_dword v[0:1], v2, off offset:64
